# p13 RWKV scan: the writer waves touch (one dword per 64 B) the P, Q-slice and decay operators of chunk st+12 so the scanning waves' loads hit the local L2
# baseline (speedup 1.0000x reference)
.LBB0_1345:
	s_and_b64 vcc, exec, s[6:7]
	s_cbranch_vccz .LBB0_1356
	s_lshl_b32 s10, s14, 7
	s_cmp_eq_u32 s16, 0
	v_lshlrev_b32_e32 v2, 3, v1
	s_cselect_b64 s[6:7], -1, 0
	v_add_u32_e32 v4, s17, v2
	v_lshl_or_b32 v2, s13, 11, v2
	v_mov_b32_e32 v3, 0
	s_add_i32 s12, s12, 0
	v_lshl_add_u64 v[2:3], s[4:5], 0, v[2:3]
	v_lshlrev_b32_e32 v16, 7, v1
	v_mov_b32_e32 v17, 0
	v_lshl_add_u64 v[16:17], s[4:5], 0, v[16:17]
	v_add_co_u32_e32 v16, vcc, 0x4400000, v16
	s_nop 1
	v_addc_co_u32_e32 v17, vcc, 0, v17, vcc
	v_and_b32_e32 v18, 15, v1
	v_lshlrev_b32_e32 v18, 7, v18
	v_lshl_or_b32 v18, s13, 11, v18
	v_mov_b32_e32 v19, 0
	v_lshl_add_u64 v[18:19], s[4:5], 0, v[18:19]
	v_add_co_u32_e32 v18, vcc, 0x8400000, v18
	s_nop 1
	v_addc_co_u32_e32 v19, vcc, 0, v19, vcc
	v_and_b32_e32 v24, 1, v1
	v_lshlrev_b32_e32 v24, 7, v24
	v_mov_b32_e32 v25, 0
	v_lshl_add_u64 v[24:25], s[4:5], 0, v[24:25]
	v_add_co_u32_e32 v24, vcc, 0x3ea00000, v24
	s_nop 1
	v_addc_co_u32_e32 v25, vcc, 0, v25, vcc
	s_cmp_eq_u32 s16, 0
	s_cselect_b32 s21, 0, -1
	s_mov_b32 s20, 0x18000
	s_xor_b32 s20, s20, s21
	s_sub_u32 s20, s20, s21
	s_mov_b64 s[8:9], 0x37200000
	s_add_i32 s2, s12, 0x10000
	s_mov_b32 s11, 0
	v_cmp_eq_u32_e64 s[0:1], 0, v1
	v_lshl_add_u64 v[2:3], v[2:3], 0, s[8:9]
	v_mov_b32_e32 v5, s2
	s_add_i32 s12, s12, 0x10020
	s_branch .LBB0_1348

.LBB0_1350:
	s_sub_i32 s2, 0x7f, s11
	s_and_b64 s[8:9], s[6:7], exec
	s_cselect_b32 s2, s11, s2
	s_add_i32 s8, s2, s10
	s_lshl_b32 s2, s11, 11
	s_and_b32 s2, s2, 0x3000
	v_add_u32_e32 v12, s2, v4
	ds_read2st64_b64 v[6:9], v12 offset1:1
	s_ashr_i32 s9, s8, 31
	s_lshl_b64 s[8:9], s[8:9], 13
	v_lshl_add_u64 v[10:11], v[2:3], 0, s[8:9]
	s_add_u32 s22, s8, s20
	s_addc_u32 s23, s9, s21
	v_lshl_add_u64 v[26:27], v[16:17], 0, s[22:23]
	global_load_dword v20, v[26:27], off
	global_load_dword v20, v[26:27], off offset:64
	v_lshl_add_u64 v[26:27], v[18:19], 0, s[22:23]
	global_load_dword v20, v[26:27], off
	global_load_dword v20, v[26:27], off offset:64
	s_ashr_i64 s[22:23], s[22:23], 5
	v_lshl_add_u64 v[26:27], v[24:25], 0, s[22:23]
	global_load_dword v20, v[26:27], off
	global_load_dword v20, v[26:27], off offset:64
	s_waitcnt lgkmcnt(0)
	global_store_dwordx2 v[10:11], v[6:7], off nt
	global_store_dwordx2 v[10:11], v[8:9], off offset:512 nt
	ds_read2st64_b64 v[6:9], v12 offset0:2 offset1:3
	s_or_b32 s13, s11, 1
	s_waitcnt lgkmcnt(0)
	global_store_dwordx2 v[10:11], v[6:7], off offset:1024 nt
	global_store_dwordx2 v[10:11], v[8:9], off offset:1536 nt
	s_waitcnt lgkmcnt(0)
	s_and_saveexec_b64 s[8:9], s[0:1]
	v_mov_b32_e32 v6, s12
	v_mov_b32_e32 v7, s13
	ds_write_b32 v6, v7
	s_or_b64 exec, exec, s[8:9]
	ds_read_b32 v6, v5
	s_waitcnt lgkmcnt(0)
	v_cmp_lt_u32_e32 vcc, s13, v6
	s_cbranch_vccnz .LBB0_1354

.LBB0_1354:
	s_sub_i32 s2, 0x7f, s13
	s_and_b64 s[8:9], s[6:7], exec
	s_cselect_b32 s2, s13, s2
	s_add_i32 s8, s2, s10
	s_lshl_b32 s2, s13, 11
	s_and_b32 s2, s2, 0x3800
	v_add_u32_e32 v10, s2, v4
	ds_read2st64_b64 v[6:9], v10 offset1:1
	s_ashr_i32 s9, s8, 31
	ds_read2st64_b64 v[10:13], v10 offset0:2 offset1:3
	s_lshl_b64 s[8:9], s[8:9], 13
	v_lshl_add_u64 v[14:15], v[2:3], 0, s[8:9]
	s_add_u32 s22, s8, s20
	s_addc_u32 s23, s9, s21
	v_lshl_add_u64 v[26:27], v[16:17], 0, s[22:23]
	global_load_dword v20, v[26:27], off
	global_load_dword v20, v[26:27], off offset:64
	v_lshl_add_u64 v[26:27], v[18:19], 0, s[22:23]
	global_load_dword v20, v[26:27], off
	global_load_dword v20, v[26:27], off offset:64
	s_ashr_i64 s[22:23], s[22:23], 5
	v_lshl_add_u64 v[26:27], v[24:25], 0, s[22:23]
	global_load_dword v20, v[26:27], off
	global_load_dword v20, v[26:27], off offset:64
	s_waitcnt lgkmcnt(1)
	global_store_dwordx2 v[14:15], v[6:7], off nt
	global_store_dwordx2 v[14:15], v[8:9], off offset:512 nt
	s_waitcnt lgkmcnt(0)
	global_store_dwordx2 v[14:15], v[10:11], off offset:1024 nt
	global_store_dwordx2 v[14:15], v[12:13], off offset:1536 nt
	s_waitcnt lgkmcnt(0)
	s_add_i32 s11, s11, 2
	s_and_saveexec_b64 s[8:9], s[0:1]
	s_cbranch_execz .LBB0_1347
	v_mov_b32_e32 v6, s12
	v_mov_b32_e32 v7, s11
	ds_write_b32 v6, v7
	s_branch .LBB0_1347

.LBB0_3663:
	s_and_b64 vcc, exec, s[6:7]
	s_cbranch_vccz .LBB0_3674
	s_lshl_b32 s11, s11, 7
	v_lshlrev_b32_e32 v2, 3, v1
	s_cmp_eq_u32 s18, 0
	v_add_u32_e32 v4, s19, v2
	v_lshl_or_b32 v2, s10, 11, v2
	v_mov_b32_e32 v3, 0
	s_cselect_b64 s[6:7], -1, 0
	v_lshl_add_u64 v[2:3], s[4:5], 0, v[2:3]
	v_lshlrev_b32_e32 v16, 7, v1
	v_mov_b32_e32 v17, 0
	v_lshl_add_u64 v[16:17], s[4:5], 0, v[16:17]
	v_add_co_u32_e32 v16, vcc, 0x4400000, v16
	s_nop 1
	v_addc_co_u32_e32 v17, vcc, 0, v17, vcc
	v_and_b32_e32 v18, 15, v1
	v_lshlrev_b32_e32 v18, 7, v18
	v_lshl_or_b32 v18, s10, 11, v18
	v_mov_b32_e32 v19, 0
	v_lshl_add_u64 v[18:19], s[4:5], 0, v[18:19]
	v_add_co_u32_e32 v18, vcc, 0x8400000, v18
	s_nop 1
	v_addc_co_u32_e32 v19, vcc, 0, v19, vcc
	v_and_b32_e32 v24, 1, v1
	v_lshlrev_b32_e32 v24, 7, v24
	v_mov_b32_e32 v25, 0
	v_lshl_add_u64 v[24:25], s[4:5], 0, v[24:25]
	v_add_co_u32_e32 v24, vcc, 0x3ea00000, v24
	s_nop 1
	v_addc_co_u32_e32 v25, vcc, 0, v25, vcc
	s_cmp_eq_u32 s18, 0
	s_cselect_b32 s21, 0, -1
	s_mov_b32 s20, 0x18000
	s_xor_b32 s20, s20, s21
	s_sub_u32 s20, s20, s21
	s_mov_b64 s[2:3], 0x37200000
	s_add_i32 s9, s9, 0
	v_lshl_add_u64 v[2:3], v[2:3], 0, s[2:3]
	s_add_i32 s2, s9, 0x10000
	s_mov_b32 s14, 0
	v_cmp_eq_u32_e64 s[0:1], 0, v1
	v_mov_b32_e32 v5, s2
	s_add_i32 s9, s9, 0x10020
	s_branch .LBB0_3666

.LBB0_3668:
	s_sub_i32 s10, 0x7f, s14
	s_and_b64 s[2:3], s[6:7], exec
	s_cselect_b32 s2, s14, s10
	s_lshl_b32 s3, s14, 11
	s_and_b32 s3, s3, 0x3000
	v_add_u32_e32 v10, s3, v4
	ds_read2st64_b64 v[6:9], v10 offset1:1
	s_add_i32 s2, s2, s11
	s_ashr_i32 s3, s2, 31
	ds_read2st64_b64 v[10:13], v10 offset0:2 offset1:3
	s_lshl_b64 s[2:3], s[2:3], 13
	v_lshl_add_u64 v[14:15], v[2:3], 0, s[2:3]
	s_add_u32 s22, s2, s20
	s_addc_u32 s23, s3, s21
	v_lshl_add_u64 v[26:27], v[16:17], 0, s[22:23]
	global_load_dword v20, v[26:27], off
	global_load_dword v20, v[26:27], off offset:64
	v_lshl_add_u64 v[26:27], v[18:19], 0, s[22:23]
	global_load_dword v20, v[26:27], off
	global_load_dword v20, v[26:27], off offset:64
	s_ashr_i64 s[22:23], s[22:23], 5
	v_lshl_add_u64 v[26:27], v[24:25], 0, s[22:23]
	global_load_dword v20, v[26:27], off
	global_load_dword v20, v[26:27], off offset:64
	s_waitcnt lgkmcnt(1)
	global_store_dwordx2 v[14:15], v[6:7], off nt
	global_store_dwordx2 v[14:15], v[8:9], off offset:512 nt
	s_waitcnt lgkmcnt(0)
	global_store_dwordx2 v[14:15], v[10:11], off offset:1024 nt
	global_store_dwordx2 v[14:15], v[12:13], off offset:1536 nt
	s_waitcnt lgkmcnt(0)
	s_or_b32 s10, s14, 1
	s_and_saveexec_b64 s[12:13], s[0:1]
	v_mov_b32_e32 v6, s9
	v_mov_b32_e32 v7, s10
	ds_write_b32 v6, v7
	s_or_b64 exec, exec, s[12:13]
	ds_read_b32 v6, v5
	s_waitcnt lgkmcnt(0)
	v_cmp_lt_u32_e32 vcc, s10, v6
	s_cbranch_vccnz .LBB0_3672

.LBB0_3672:
	s_sub_i32 s12, 0x7f, s10
	s_and_b64 s[2:3], s[6:7], exec
	s_cselect_b32 s2, s10, s12
	s_lshl_b32 s3, s10, 11
	s_and_b32 s3, s3, 0x3800
	v_add_u32_e32 v10, s3, v4
	ds_read2st64_b64 v[6:9], v10 offset1:1
	s_add_i32 s2, s2, s11
	s_ashr_i32 s3, s2, 31
	ds_read2st64_b64 v[10:13], v10 offset0:2 offset1:3
	s_lshl_b64 s[2:3], s[2:3], 13
	v_lshl_add_u64 v[14:15], v[2:3], 0, s[2:3]
	s_add_u32 s22, s2, s20
	s_addc_u32 s23, s3, s21
	v_lshl_add_u64 v[26:27], v[16:17], 0, s[22:23]
	global_load_dword v20, v[26:27], off
	global_load_dword v20, v[26:27], off offset:64
	v_lshl_add_u64 v[26:27], v[18:19], 0, s[22:23]
	global_load_dword v20, v[26:27], off
	global_load_dword v20, v[26:27], off offset:64
	s_ashr_i64 s[22:23], s[22:23], 5
	v_lshl_add_u64 v[26:27], v[24:25], 0, s[22:23]
	global_load_dword v20, v[26:27], off
	global_load_dword v20, v[26:27], off offset:64
	s_waitcnt lgkmcnt(1)
	global_store_dwordx2 v[14:15], v[6:7], off nt
	global_store_dwordx2 v[14:15], v[8:9], off offset:512 nt
	s_waitcnt lgkmcnt(0)
	global_store_dwordx2 v[14:15], v[10:11], off offset:1024 nt
	global_store_dwordx2 v[14:15], v[12:13], off offset:1536 nt
	s_waitcnt lgkmcnt(0)
	s_add_i32 s14, s14, 2
	s_and_saveexec_b64 s[12:13], s[0:1]
	s_cbranch_execz .LBB0_3665
	v_mov_b32_e32 v6, s9
	v_mov_b32_e32 v7, s14
	ds_write_b32 v6, v7
	s_branch .LBB0_3665
